# all four layers' expert weight conversion now done at the grid barriers (two items per wave at lockstep barriers), prologue keeps only the small weights
# speedup vs baseline: 1.0066x; 1.0048x over previous
.LBB0_133:
	s_add_i32 s46, s41, s33
	s_add_i32 s2, s46, 0xfffff750
	s_cmp_lt_i32 s2, 0
	s_cbranch_scc1 .Lp0_noskip
	s_cmp_lt_i32 s2, 0x6000
	s_cbranch_scc1 .Lp0_skip
	s_add_i32 s2, s2, 0xffff9750
	s_cmp_lt_i32 s2, 0
	s_cbranch_scc1 .Lp0_noskip
	s_cmp_lt_i32 s2, 0x6000
	s_cbranch_scc1 .Lp0_skip
	s_add_i32 s2, s2, 0xffff9750
	s_cmp_lt_i32 s2, 0
	s_cbranch_scc1 .Lp0_noskip
	s_cmp_lt_i32 s2, 0x6000
	s_cbranch_scc1 .Lp0_skip
	s_add_i32 s2, s2, 0xffff9750
	s_cmp_lt_i32 s2, 0
	s_cbranch_scc1 .Lp0_noskip
	s_cmp_lt_i32 s2, 0x6000
	s_cbranch_scc1 .Lp0_skip
	s_branch .Lp0_noskip

.Lcvt_post:
	s_mov_b64 exec, -1
	v_lshrrev_b32_e32 v2, 6, v0
	v_and_b32_e32 v3, 63, v0
	s_nop 0
	v_readfirstlane_b32 s25, v2
	s_nop 3
	v_lshrrev_b32_e32 v4, 3, v3
	v_and_b32_e32 v5, 7, v3
	v_mul_u32_u24_e32 v7, 17, v4
	v_and_b32_e32 v8, 3, v3
	v_lshl_add_u32 v7, v8, 2, v7
	v_lshlrev_b32_e32 v7, 2, v7
	v_mul_u32_u24_e32 v8, 0x110, v5
	v_add_lshl_u32 v8, v8, v4, 2
	s_mul_i32 s17, s25, 0x2200
	v_add_u32_e32 v7, s17, v7
	v_add_u32_e32 v8, s17, v8
	v_lshlrev_b32_e32 v9, 10, v4
	v_lshl_add_u32 v9, v5, 4, v9
	v_add_u32_e32 v10, 0x2000, v9
	s_cmp_eq_u32 s31, 5
	s_cbranch_scc0 .Lcvt_t3
	s_cmp_ge_u32 s62, 3
	s_cbranch_scc1 .Lcvt_ret
	s_sub_i32 s27, s80, 16
	s_cmp_lt_i32 s27, 0
	s_cbranch_scc1 .Lcvt_ret
	s_mov_b32 s26, 3
	s_movk_i32 s30, 0
	s_movk_i32 s4, 5040
	s_mov_b32 s24, s62
	s_branch .Lcvt_go
.Lcvt_t3:
	s_cmp_eq_u32 s31, 3
	s_cbranch_scc0 .Lcvt_t10
	s_sub_i32 s27, s63, 208
	s_cmp_lt_i32 s27, 0
	s_cbranch_scc1 .Lcvt_ret
	s_mov_b32 s26, 1
	s_movk_i32 s30, 5040
	s_movk_i32 s4, 5376
	s_mov_b32 s24, s62
	s_branch .Lcvt_go
.Lcvt_t10:
	s_cmp_eq_u32 s31, 10
	s_cbranch_scc0 .Lcvt_lock
	s_cmp_ge_u32 s62, 3
	s_cbranch_scc1 .Lcvt_ret
	s_sub_i32 s27, s63, 136
	s_cmp_lt_i32 s27, 0
	s_cbranch_scc1 .Lcvt_ret
	s_mov_b32 s26, 4
	s_movk_i32 s30, 5376
	s_movk_i32 s4, 8736
	s_add_i32 s24, s62, 1
.Lcvt_go:
	s_mul_i32 s27, s27, 7
	s_add_i32 s27, s27, s25
	s_add_i32 s27, s27, -1
	s_mul_i32 s27, s27, s26
	s_add_i32 s30, s30, s27
	s_mov_b32 s27, s24
	s_mov_b32 s25, 0
	s_branch .Lcvt_item
.Lcvt_lock:
	s_mov_b32 s27, -1
	s_cmp_eq_u32 s31, 0
	s_cselect_b32 s27, 0, s27
	s_cmp_eq_u32 s31, 1
	s_cselect_b32 s27, 1, s27
	s_cmp_eq_u32 s31, 2
	s_cselect_b32 s27, 2, s27
	s_cmp_eq_u32 s31, 4
	s_cselect_b32 s27, 3, s27
	s_cmp_eq_u32 s31, 6
	s_cselect_b32 s27, 4, s27
	s_cmp_eq_u32 s31, 7
	s_cselect_b32 s27, 5, s27
	s_cmp_eq_u32 s31, 8
	s_cselect_b32 s27, 6, s27
	s_cmp_eq_u32 s31, 9
	s_cselect_b32 s27, 7, s27
	s_cmp_lt_i32 s27, 0
	s_cbranch_scc1 .Lcvt_ret
	s_mul_i32 s26, s62, 8
	s_add_i32 s27, s27, s26
	s_mul_i32 s27, s27, 3584
	s_mul_i32 s26, s80, 7
	s_add_i32 s26, s26, s25
	s_add_i32 s26, s26, -1
	s_lshl_b32 s26, s26, 1
	s_add_i32 s30, s27, s26
	s_mov_b32 s26, 2
	s_mov_b32 s4, 71760
	s_mov_b32 s25, 1
.Lcvt_item:
	s_cmp_ge_u32 s30, s4
	s_cbranch_scc1 .Lcvt_ret
	s_mov_b32 s6, s27
	s_mov_b32 s5, s30
	s_cmp_eq_u32 s25, 0
	s_cbranch_scc1 .Lcvt_dec
	s_cmp_lt_u32 s30, 19200
	s_cbranch_scc0 .Lcvt_lk0
	s_mov_b32 s6, 0
	s_sub_i32 s5, s30, 0
	s_add_i32 s5, s5, 5376
	s_branch .Lcvt_dec
.Lcvt_lk0:
	s_cmp_lt_u32 s30, 35040
	s_cbranch_scc0 .Lcvt_lk1
	s_mov_b32 s6, 1
	s_sub_i32 s5, s30, 19200
	s_add_i32 s5, s5, 8736
	s_branch .Lcvt_dec
.Lcvt_lk1:
	s_cmp_lt_u32 s30, 50880
	s_cbranch_scc0 .Lcvt_lk2
	s_mov_b32 s6, 2
	s_sub_i32 s5, s30, 35040
	s_add_i32 s5, s5, 8736
	s_branch .Lcvt_dec
.Lcvt_lk2:
	s_cmp_lt_u32 s30, 71760
	s_cbranch_scc0 .Lcvt_lk3
	s_mov_b32 s6, 3
	s_sub_i32 s5, s30, 50880
	s_cmp_lt_u32 s5, 5040
	s_cbranch_scc1 .Lcvt_dec
	s_add_i32 s5, s5, 3696
	s_branch .Lcvt_dec

.Lcvt_dec:
	s_lshr_b32 s7, s5, 8
	s_mul_i32 s7, s7, 0xaaab
	s_lshr_b32 s7, s7, 17
	s_mul_i32 s8, s7, 0x300
	s_sub_i32 s8, s5, s8
	s_lshl_b32 s9, s6, 5
	s_add_i32 s9, s9, s7
	s_load_dwordx2 s[2:3], s[0:1], 0x100
	s_mov_b32 s18, s9
	s_mov_b32 s19, 0
	s_cmp_lt_u32 s8, 0x200
	s_cbranch_scc0 .Lcvt_dn
	s_load_dwordx2 s[10:11], s[0:1], 0xd8
	s_lshr_b32 s12, s8, 6
	s_and_b32 s13, s8, 63
	s_lshr_b32 s14, s13, 2
	s_and_b32 s14, s14, 7
	s_lshl_b32 s14, s14, 3
	s_and_b32 s15, s13, 3
	s_add_i32 s14, s14, s15
	s_lshr_b32 s15, s13, 5
	s_lshl_b32 s15, s15, 2
	s_add_i32 s14, s14, s15
	s_mov_b32 s16, 13
	s_lshl_b64 s[20:21], s[18:19], 23
	s_lshl_b64 s[22:23], s[18:19], 21
	s_mov_b32 s24, 0x6000000
	s_branch .Lcvt_common
